# attention key loop: two 64-key tiles per workgroup barrier (four LDS tile images), second tile's first K fragments read under the first tile's last PV MFMAs (v27 otherwise)
# baseline (speedup 1.0000x reference)
.LBB0_754:
	s_or_b64 exec, exec, s[14:15]
	s_waitcnt vmcnt(17)
	v_mad_u64_u32 v[106:107], s[14:15], v13, s8, v[14:15]
	v_mul_lo_u32 v20, v20, s25
	v_lshl_add_u32 v21, v106, 1, 0
	s_waitcnt vmcnt(1)
	ds_write_b128 v21, v[6:9] offset:64
	v_lshl_add_u32 v6, v128, 1, 0
	v_add_u32_e32 v129, v194, v20
	s_waitcnt vmcnt(0)
	ds_write_b128 v6, v[2:5] offset:64
	s_and_saveexec_b64 s[14:15], s[36:37]
	s_xor_b64 s[14:15], exec, s[14:15]
	v_add_u32_e32 v129, v194, v20
	s_andn2_saveexec_b64 s[14:15], s[14:15]
	v_lshl_add_u32 v2, v129, 1, 0
	ds_write_b128 v2, v[90:93] offset:13376
	s_or_b64 exec, exec, s[14:15]
	v_mad_i64_i32 v[2:3], s[14:15], v13, s24, 0
	s_add_i32 s70, s67, s68
	s_lshl_b64 s[14:15], s[70:71], 1
	s_add_u32 s14, s34, s14
	v_lshl_add_u64 v[4:5], v[194:195], 1, v[16:17]
	s_addc_u32 s15, s35, s15
	v_lshl_add_u64 v[4:5], s[14:15], 0, v[4:5]
	v_mad_u64_u32 v[2:3], s[14:15], s9, v229, v[2:3]
	v_mad_u64_u32 v[2:3], s[14:15], s66, v230, v[2:3]
	v_lshl_add_u64 v[2:3], v[14:15], 1, v[2:3]
	v_lshlrev_b32_e32 v194, 1, v12
	v_lshl_add_u64 v[2:3], s[42:43], 0, v[2:3]
	v_mov_b32_e32 v105, 0
	v_ashrrev_i32_e32 v103, 31, v102
	v_lshlrev_b32_e32 v104, 3, v19
	v_mul_u32_u24_e32 v130, 0x68, v18
	v_mul_u32_u24_e32 v107, 0x48, v18
	s_mov_b32 s30, 1
	v_lshl_add_u64 v[108:109], v[4:5], 0, s[10:11]
	v_lshl_add_u64 v[110:111], v[10:11], 0, v[194:195]
	v_lshl_add_u64 v[112:113], v[2:3], 0, s[12:13]
	v_mov_b32_e32 v18, 0
	v_mov_b32_e32 v19, v105
	v_mov_b32_e32 v20, v105
	v_mov_b32_e32 v21, v105
	v_mov_b32_e32 v22, v105
	v_mov_b32_e32 v23, v105
	v_mov_b32_e32 v24, v105
	v_mov_b32_e32 v25, v105
	v_mov_b32_e32 v26, v105
	v_mov_b32_e32 v27, v105
	v_mov_b32_e32 v28, v105
	v_mov_b32_e32 v29, v105
	v_mov_b32_e32 v30, v105
	v_mov_b32_e32 v31, v105
	v_mov_b32_e32 v32, v105
	v_mov_b32_e32 v33, v105
	v_mov_b32_e32 v2, 0
	v_mov_b32_e32 v3, v105
	v_mov_b32_e32 v4, v105
	v_mov_b32_e32 v5, v105
	v_mov_b32_e32 v6, v105
	v_mov_b32_e32 v7, v105
	v_mov_b32_e32 v8, v105
	v_mov_b32_e32 v9, v105
	v_mov_b32_e32 v10, v105
	v_mov_b32_e32 v11, v105
	v_mov_b32_e32 v12, v105
	v_mov_b32_e32 v13, v105
	v_mov_b32_e32 v14, v105
	v_mov_b32_e32 v15, v105
	v_mov_b32_e32 v16, v105
	v_mov_b32_e32 v17, v105
	s_waitcnt lgkmcnt(0)
	s_barrier
	s_cmp_lg_u64 vcc, 0
	s_cselect_b32 s43, 1, 0
	v_add_lshl_u32 v130, v130, v104, 1
	v_add_lshl_u32 v107, v107, v104, 1
	v_lshlrev_b32_e32 v106, 1, v106
	v_lshlrev_b32_e32 v128, 1, v128
	v_lshlrev_b32_e32 v129, 1, v129
	v_mov_b32_e32 v145, 0
	global_load_dwordx4 v[98:101], v[112:113], off
	global_load_dwordx4 v[94:97], v[110:111], off
	s_cmp_lg_u32 s43, 0
	s_cbranch_scc0 .Lfa_pre_nov
	global_load_dwordx4 v[90:93], v[108:109], off
.Lfa_pre_nov:
	v_lshl_add_u64 v[112:113], v[112:113], 0, s[12:13]
	v_lshl_add_u64 v[110:111], v[110:111], 0, v[194:195]
	v_lshl_add_u64 v[108:109], v[108:109], 0, s[10:11]
	v_add_u32_e32 v182, 0xb000, v130
	v_add_u32_e32 v183, 0xb000, v107
	v_add_u32_e32 v184, 0xb000, v106
	v_add_u32_e32 v185, 0xb000, v128
	v_add_u32_e32 v186, 0xb000, v129
	v_mov_b32_e32 v50, 0
	v_mov_b32_e32 v51, 0
	v_mov_b32_e32 v52, 0
	v_mov_b32_e32 v53, 0
	v_mov_b32_e32 v54, 0
	v_mov_b32_e32 v55, 0
	v_mov_b32_e32 v56, 0
	v_mov_b32_e32 v57, 0
	v_mov_b32_e32 v58, 0
	v_mov_b32_e32 v59, 0
	v_mov_b32_e32 v60, 0
	v_mov_b32_e32 v61, 0
	v_mov_b32_e32 v62, 0
	v_mov_b32_e32 v63, 0
	v_mov_b32_e32 v64, 0
	v_mov_b32_e32 v65, 0
	s_waitcnt vmcnt(0)
	ds_write_b128 v106, v[98:101] offset:22592
	ds_write_b128 v128, v[94:97] offset:22592
	s_cmp_lg_u32 s43, 0
	s_cbranch_scc0 .Lfa_pre_nowv
	ds_write_b128 v129, v[90:93] offset:35904
.Lfa_pre_nowv:
	s_waitcnt lgkmcnt(0)
	s_barrier
	s_mov_b32 s30, 0
.Lfa_loop:
.Lfa_pair_0:
	s_add_i32 s31, s30, 2
	s_cmp_lt_u32 s31, s65
	s_cbranch_scc0 .Lfa_noload_00
	global_load_dwordx4 v[98:101], v[112:113], off
	global_load_dwordx4 v[94:97], v[110:111], off
	s_cmp_lg_u32 s43, 0
	s_cbranch_scc0 .Lfa_noload_00
	global_load_dwordx4 v[90:93], v[108:109], off
.Lfa_noload_00:
	ds_read_b128 v[114:117], v130 offset:64
	ds_read_b128 v[118:121], v130 offset:96
	ds_read_b128 v[122:125], v130 offset:128
	ds_read_b128 v[132:135], v130 offset:160
	ds_read_b128 v[136:139], v130 offset:192
	ds_read_b128 v[140:143], v130 offset:224
	ds_read_b128 v[146:149], v130 offset:6720
	ds_read_b128 v[150:153], v130 offset:6752
	s_waitcnt lgkmcnt(7)
	v_mfma_f32_32x32x16_bf16 v[34:49], v[114:117], v[86:89], 0
	v_add_f32_e32 v105, v105, v50
	v_add_f32_e32 v145, v145, v51
	v_add_f32_e32 v105, v105, v52
	ds_read_b128 v[154:157], v130 offset:6784
	s_waitcnt lgkmcnt(7)
	v_mfma_f32_32x32x16_bf16 v[34:49], v[118:121], v[82:85], v[34:49]
	v_add_f32_e32 v145, v145, v53
	v_add_f32_e32 v105, v105, v54
	v_add_f32_e32 v145, v145, v55
	ds_read_b128 v[158:161], v130 offset:6816
	s_waitcnt lgkmcnt(7)
	v_mfma_f32_32x32x16_bf16 v[34:49], v[122:125], v[78:81], v[34:49]
	v_add_f32_e32 v105, v105, v56
	v_add_f32_e32 v145, v145, v57
	v_add_f32_e32 v105, v105, v58
	ds_read_b128 v[162:165], v130 offset:6848
	s_waitcnt lgkmcnt(7)
	v_mfma_f32_32x32x16_bf16 v[34:49], v[132:135], v[74:77], v[34:49]
	v_add_f32_e32 v145, v145, v59
	v_add_f32_e32 v105, v105, v60
	v_add_f32_e32 v145, v145, v61
	ds_read_b128 v[166:169], v130 offset:6880
	s_waitcnt lgkmcnt(7)
	v_mfma_f32_32x32x16_bf16 v[34:49], v[136:139], v[70:73], v[34:49]
	v_add_f32_e32 v105, v105, v62
	v_add_f32_e32 v145, v145, v63
	s_waitcnt lgkmcnt(6)
	v_mfma_f32_32x32x16_bf16 v[34:49], v[140:143], v[66:69], v[34:49]
	v_add_f32_e32 v105, v105, v64
	v_add_f32_e32 v145, v145, v65
	s_waitcnt lgkmcnt(5)
	v_mfma_f32_32x32x16_bf16 v[50:65], v[146:149], v[86:89], 0
	ds_read_b128 v[114:117], v107 offset:13376
	ds_read_b128 v[118:121], v107 offset:17984
	ds_read_b128 v[122:125], v107 offset:13408
	ds_read_b128 v[132:135], v107 offset:18016
	ds_read_b128 v[136:139], v107 offset:13440
	ds_read_b128 v[140:143], v107 offset:18048
	ds_read_b128 v[146:149], v107 offset:13472
	s_waitcnt lgkmcnt(11)
	v_mfma_f32_32x32x16_bf16 v[50:65], v[150:153], v[82:85], v[50:65]
	ds_read_b128 v[150:153], v107 offset:18080
	v_lshl_add_u64 v[112:113], v[112:113], 0, s[12:13]
	v_lshl_add_u64 v[110:111], v[110:111], 0, v[194:195]
	v_lshl_add_u64 v[108:109], v[108:109], 0, s[10:11]
	v_exp_f32_e32 v34, v34
	v_exp_f32_e32 v35, v35
	s_waitcnt lgkmcnt(11)
	v_mfma_f32_32x32x16_bf16 v[50:65], v[154:157], v[78:81], v[50:65]
	v_exp_f32_e32 v36, v36
	v_exp_f32_e32 v37, v37
	v_exp_f32_e32 v38, v38
	s_waitcnt lgkmcnt(10)
	v_mfma_f32_32x32x16_bf16 v[50:65], v[158:161], v[74:77], v[50:65]
	v_exp_f32_e32 v39, v39
	v_exp_f32_e32 v40, v40
	v_exp_f32_e32 v41, v41
	v_cvt_pk_bf16_f32 v154, v34, v35
	s_waitcnt lgkmcnt(9)
	v_mfma_f32_32x32x16_bf16 v[50:65], v[162:165], v[70:73], v[50:65]
	v_cvt_pk_bf16_f32 v155, v36, v37
	v_cvt_pk_bf16_f32 v156, v38, v39
	v_exp_f32_e32 v42, v42
	v_exp_f32_e32 v43, v43
	s_waitcnt lgkmcnt(8)
	v_mfma_f32_32x32x16_bf16 v[50:65], v[166:169], v[66:69], v[50:65]
	v_cvt_pk_bf16_f32 v157, v40, v41
	v_exp_f32_e32 v44, v44
	v_exp_f32_e32 v45, v45
	v_exp_f32_e32 v46, v46
	s_waitcnt lgkmcnt(7)
	v_mfma_f32_32x32x16_bf16 v[18:33], v[114:117], v[154:157], v[18:33]
	v_exp_f32_e32 v47, v47
	v_exp_f32_e32 v48, v48
	v_exp_f32_e32 v49, v49
	v_cvt_pk_bf16_f32 v158, v42, v43
	s_waitcnt lgkmcnt(6)
	v_mfma_f32_32x32x16_bf16 v[2:17], v[118:121], v[154:157], v[2:17]
	v_cvt_pk_bf16_f32 v159, v44, v45
	v_cvt_pk_bf16_f32 v160, v46, v47
	v_cvt_pk_bf16_f32 v161, v48, v49
	v_add_f32_e32 v105, v105, v34
	v_add_f32_e32 v145, v145, v35
	v_add_f32_e32 v105, v105, v36
	v_exp_f32_e32 v50, v50
	s_waitcnt lgkmcnt(5)
	v_mfma_f32_32x32x16_bf16 v[18:33], v[122:125], v[158:161], v[18:33]
	v_exp_f32_e32 v51, v51
	v_exp_f32_e32 v52, v52
	v_exp_f32_e32 v53, v53
	s_waitcnt lgkmcnt(4)
	v_mfma_f32_32x32x16_bf16 v[2:17], v[132:135], v[158:161], v[2:17]
	v_exp_f32_e32 v54, v54
	v_exp_f32_e32 v55, v55
	v_exp_f32_e32 v56, v56
	v_exp_f32_e32 v57, v57
	v_cvt_pk_bf16_f32 v162, v50, v51
	v_cvt_pk_bf16_f32 v163, v52, v53
	v_cvt_pk_bf16_f32 v164, v54, v55
	v_cvt_pk_bf16_f32 v165, v56, v57
	v_add_f32_e32 v145, v145, v37
	v_add_f32_e32 v105, v105, v38
	s_waitcnt lgkmcnt(3)
	v_mfma_f32_32x32x16_bf16 v[18:33], v[136:139], v[162:165], v[18:33]
	v_exp_f32_e32 v58, v58
	v_exp_f32_e32 v59, v59
	v_exp_f32_e32 v60, v60
	s_waitcnt lgkmcnt(2)
	v_mfma_f32_32x32x16_bf16 v[2:17], v[140:143], v[162:165], v[2:17]
	ds_read_b128 v[114:117], v130 offset:22592
	ds_read_b128 v[118:121], v130 offset:22624
	ds_read_b128 v[122:125], v130 offset:22656
	ds_read_b128 v[132:135], v130 offset:22688
	v_exp_f32_e32 v61, v61
	v_exp_f32_e32 v62, v62
	v_exp_f32_e32 v63, v63
	v_exp_f32_e32 v64, v64
	v_exp_f32_e32 v65, v65
	v_cvt_pk_bf16_f32 v166, v58, v59
	v_cvt_pk_bf16_f32 v167, v60, v61
	v_cvt_pk_bf16_f32 v168, v62, v63
	v_cvt_pk_bf16_f32 v169, v64, v65
	v_add_f32_e32 v145, v145, v39
	v_add_f32_e32 v105, v105, v40
	s_waitcnt lgkmcnt(5)
	v_mfma_f32_32x32x16_bf16 v[18:33], v[146:149], v[166:169], v[18:33]
	v_add_f32_e32 v145, v145, v41
	v_add_f32_e32 v105, v105, v42
	v_add_f32_e32 v145, v145, v43
	v_add_f32_e32 v105, v105, v44
	v_add_f32_e32 v145, v145, v45
	s_waitcnt lgkmcnt(4)
	v_mfma_f32_32x32x16_bf16 v[2:17], v[150:153], v[166:169], v[2:17]
	v_add_f32_e32 v105, v105, v46
	v_add_f32_e32 v145, v145, v47
	v_add_f32_e32 v105, v105, v48
	v_add_f32_e32 v145, v145, v49
	s_cmp_lt_u32 s31, s65
	s_cbranch_scc0 .Lfa_noload_01
	global_load_dwordx4 v[170:173], v[112:113], off
	global_load_dwordx4 v[174:177], v[110:111], off
	s_cmp_lg_u32 s43, 0
	s_cbranch_scc0 .Lfa_noload_01
	global_load_dwordx4 v[178:181], v[108:109], off
.Lfa_noload_01:
	ds_read_b128 v[136:139], v130 offset:22720
	ds_read_b128 v[140:143], v130 offset:22752
	ds_read_b128 v[146:149], v130 offset:29248
	ds_read_b128 v[150:153], v130 offset:29280
	s_waitcnt lgkmcnt(7)
	v_mfma_f32_32x32x16_bf16 v[34:49], v[114:117], v[86:89], 0
	v_add_f32_e32 v105, v105, v50
	v_add_f32_e32 v145, v145, v51
	v_add_f32_e32 v105, v105, v52
	ds_read_b128 v[154:157], v130 offset:29312
	s_waitcnt lgkmcnt(7)
	v_mfma_f32_32x32x16_bf16 v[34:49], v[118:121], v[82:85], v[34:49]
	v_add_f32_e32 v145, v145, v53
	v_add_f32_e32 v105, v105, v54
	v_add_f32_e32 v145, v145, v55
	ds_read_b128 v[158:161], v130 offset:29344
	s_waitcnt lgkmcnt(7)
	v_mfma_f32_32x32x16_bf16 v[34:49], v[122:125], v[78:81], v[34:49]
	v_add_f32_e32 v105, v105, v56
	v_add_f32_e32 v145, v145, v57
	v_add_f32_e32 v105, v105, v58
	ds_read_b128 v[162:165], v130 offset:29376
	s_waitcnt lgkmcnt(7)
	v_mfma_f32_32x32x16_bf16 v[34:49], v[132:135], v[74:77], v[34:49]
	v_add_f32_e32 v145, v145, v59
	v_add_f32_e32 v105, v105, v60
	v_add_f32_e32 v145, v145, v61
	ds_read_b128 v[166:169], v130 offset:29408
	s_waitcnt lgkmcnt(7)
	v_mfma_f32_32x32x16_bf16 v[34:49], v[136:139], v[70:73], v[34:49]
	v_add_f32_e32 v105, v105, v62
	v_add_f32_e32 v145, v145, v63
	s_waitcnt lgkmcnt(6)
	v_mfma_f32_32x32x16_bf16 v[34:49], v[140:143], v[66:69], v[34:49]
	v_add_f32_e32 v105, v105, v64
	v_add_f32_e32 v145, v145, v65
	s_waitcnt lgkmcnt(5)
	v_mfma_f32_32x32x16_bf16 v[50:65], v[146:149], v[86:89], 0
	ds_read_b128 v[114:117], v107 offset:35904
	ds_read_b128 v[118:121], v107 offset:40512
	ds_read_b128 v[122:125], v107 offset:35936
	ds_read_b128 v[132:135], v107 offset:40544
	ds_read_b128 v[136:139], v107 offset:35968
	ds_read_b128 v[140:143], v107 offset:40576
	ds_read_b128 v[146:149], v107 offset:36000
	s_waitcnt lgkmcnt(11)
	v_mfma_f32_32x32x16_bf16 v[50:65], v[150:153], v[82:85], v[50:65]
	ds_read_b128 v[150:153], v107 offset:40608
	v_lshl_add_u64 v[112:113], v[112:113], 0, s[12:13]
	v_lshl_add_u64 v[110:111], v[110:111], 0, v[194:195]
	v_lshl_add_u64 v[108:109], v[108:109], 0, s[10:11]
	v_exp_f32_e32 v34, v34
	v_exp_f32_e32 v35, v35
	s_waitcnt lgkmcnt(11)
	v_mfma_f32_32x32x16_bf16 v[50:65], v[154:157], v[78:81], v[50:65]
	v_exp_f32_e32 v36, v36
	v_exp_f32_e32 v37, v37
	v_exp_f32_e32 v38, v38
	s_waitcnt lgkmcnt(10)
	v_mfma_f32_32x32x16_bf16 v[50:65], v[158:161], v[74:77], v[50:65]
	v_exp_f32_e32 v39, v39
	v_exp_f32_e32 v40, v40
	v_exp_f32_e32 v41, v41
	v_cvt_pk_bf16_f32 v154, v34, v35
	s_waitcnt lgkmcnt(9)
	v_mfma_f32_32x32x16_bf16 v[50:65], v[162:165], v[70:73], v[50:65]
	v_cvt_pk_bf16_f32 v155, v36, v37
	v_cvt_pk_bf16_f32 v156, v38, v39
	v_exp_f32_e32 v42, v42
	v_exp_f32_e32 v43, v43
	s_waitcnt lgkmcnt(8)
	v_mfma_f32_32x32x16_bf16 v[50:65], v[166:169], v[66:69], v[50:65]
	v_cvt_pk_bf16_f32 v157, v40, v41
	v_exp_f32_e32 v44, v44
	v_exp_f32_e32 v45, v45
	v_exp_f32_e32 v46, v46
	s_waitcnt lgkmcnt(7)
	v_mfma_f32_32x32x16_bf16 v[18:33], v[114:117], v[154:157], v[18:33]
	v_exp_f32_e32 v47, v47
	v_exp_f32_e32 v48, v48
	v_exp_f32_e32 v49, v49
	v_cvt_pk_bf16_f32 v158, v42, v43
	s_waitcnt lgkmcnt(6)
	v_mfma_f32_32x32x16_bf16 v[2:17], v[118:121], v[154:157], v[2:17]
	v_cvt_pk_bf16_f32 v159, v44, v45
	v_cvt_pk_bf16_f32 v160, v46, v47
	v_cvt_pk_bf16_f32 v161, v48, v49
	v_add_f32_e32 v105, v105, v34
	v_add_f32_e32 v145, v145, v35
	v_add_f32_e32 v105, v105, v36
	v_exp_f32_e32 v50, v50
	s_waitcnt lgkmcnt(5)
	v_mfma_f32_32x32x16_bf16 v[18:33], v[122:125], v[158:161], v[18:33]
	v_exp_f32_e32 v51, v51
	v_exp_f32_e32 v52, v52
	v_exp_f32_e32 v53, v53
	s_waitcnt lgkmcnt(4)
	v_mfma_f32_32x32x16_bf16 v[2:17], v[132:135], v[158:161], v[2:17]
	v_exp_f32_e32 v54, v54
	v_exp_f32_e32 v55, v55
	v_exp_f32_e32 v56, v56
	v_exp_f32_e32 v57, v57
	v_cvt_pk_bf16_f32 v162, v50, v51
	v_cvt_pk_bf16_f32 v163, v52, v53
	v_cvt_pk_bf16_f32 v164, v54, v55
	v_cvt_pk_bf16_f32 v165, v56, v57
	v_add_f32_e32 v145, v145, v37
	v_add_f32_e32 v105, v105, v38
	s_waitcnt lgkmcnt(3)
	v_mfma_f32_32x32x16_bf16 v[18:33], v[136:139], v[162:165], v[18:33]
	v_exp_f32_e32 v58, v58
	v_exp_f32_e32 v59, v59
	v_exp_f32_e32 v60, v60
	s_waitcnt lgkmcnt(2)
	v_mfma_f32_32x32x16_bf16 v[2:17], v[140:143], v[162:165], v[2:17]
	v_exp_f32_e32 v61, v61
	v_exp_f32_e32 v62, v62
	v_exp_f32_e32 v63, v63
	v_exp_f32_e32 v64, v64
	v_exp_f32_e32 v65, v65
	v_cvt_pk_bf16_f32 v166, v58, v59
	v_cvt_pk_bf16_f32 v167, v60, v61
	v_cvt_pk_bf16_f32 v168, v62, v63
	v_cvt_pk_bf16_f32 v169, v64, v65
	v_add_f32_e32 v145, v145, v39
	v_add_f32_e32 v105, v105, v40
	s_waitcnt lgkmcnt(1)
	v_mfma_f32_32x32x16_bf16 v[18:33], v[146:149], v[166:169], v[18:33]
	v_add_f32_e32 v145, v145, v41
	v_add_f32_e32 v105, v105, v42
	v_add_f32_e32 v145, v145, v43
	v_add_f32_e32 v105, v105, v44
	v_add_f32_e32 v145, v145, v45
	s_waitcnt lgkmcnt(0)
	v_mfma_f32_32x32x16_bf16 v[2:17], v[150:153], v[166:169], v[2:17]
	v_add_f32_e32 v105, v105, v46
	v_add_f32_e32 v145, v145, v47
	v_add_f32_e32 v105, v105, v48
	v_add_f32_e32 v145, v145, v49
	s_cmp_lt_u32 s31, s65
	s_cbranch_scc0 .Lfa_nowrite_0
	s_waitcnt vmcnt(0)
	ds_write_b128 v184, v[98:101] offset:64
	ds_write_b128 v185, v[94:97] offset:64
	ds_write_b128 v184, v[170:173] offset:22592
	ds_write_b128 v185, v[174:177] offset:22592
	s_cmp_lg_u32 s43, 0
	s_cbranch_scc0 .Lfa_nowrite_0
	ds_write_b128 v186, v[90:93] offset:13376
	ds_write_b128 v186, v[178:181] offset:35904

.Lfa_pair_1:
	s_add_i32 s31, s30, 2
	s_cmp_lt_u32 s31, s65
	s_cbranch_scc0 .Lfa_noload_10
	global_load_dwordx4 v[98:101], v[112:113], off
	global_load_dwordx4 v[94:97], v[110:111], off
	s_cmp_lg_u32 s43, 0
	s_cbranch_scc0 .Lfa_noload_10
	global_load_dwordx4 v[90:93], v[108:109], off
.Lfa_noload_10:
	ds_read_b128 v[114:117], v182 offset:64
	ds_read_b128 v[118:121], v182 offset:96
	ds_read_b128 v[122:125], v182 offset:128
	ds_read_b128 v[132:135], v182 offset:160
	ds_read_b128 v[136:139], v182 offset:192
	ds_read_b128 v[140:143], v182 offset:224
	ds_read_b128 v[146:149], v182 offset:6720
	ds_read_b128 v[150:153], v182 offset:6752
	s_waitcnt lgkmcnt(7)
	v_mfma_f32_32x32x16_bf16 v[34:49], v[114:117], v[86:89], 0
	v_add_f32_e32 v105, v105, v50
	v_add_f32_e32 v145, v145, v51
	v_add_f32_e32 v105, v105, v52
	ds_read_b128 v[154:157], v182 offset:6784
	s_waitcnt lgkmcnt(7)
	v_mfma_f32_32x32x16_bf16 v[34:49], v[118:121], v[82:85], v[34:49]
	v_add_f32_e32 v145, v145, v53
	v_add_f32_e32 v105, v105, v54
	v_add_f32_e32 v145, v145, v55
	ds_read_b128 v[158:161], v182 offset:6816
	s_waitcnt lgkmcnt(7)
	v_mfma_f32_32x32x16_bf16 v[34:49], v[122:125], v[78:81], v[34:49]
	v_add_f32_e32 v105, v105, v56
	v_add_f32_e32 v145, v145, v57
	v_add_f32_e32 v105, v105, v58
	ds_read_b128 v[162:165], v182 offset:6848
	s_waitcnt lgkmcnt(7)
	v_mfma_f32_32x32x16_bf16 v[34:49], v[132:135], v[74:77], v[34:49]
	v_add_f32_e32 v145, v145, v59
	v_add_f32_e32 v105, v105, v60
	v_add_f32_e32 v145, v145, v61
	ds_read_b128 v[166:169], v182 offset:6880
	s_waitcnt lgkmcnt(7)
	v_mfma_f32_32x32x16_bf16 v[34:49], v[136:139], v[70:73], v[34:49]
	v_add_f32_e32 v105, v105, v62
	v_add_f32_e32 v145, v145, v63
	s_waitcnt lgkmcnt(6)
	v_mfma_f32_32x32x16_bf16 v[34:49], v[140:143], v[66:69], v[34:49]
	v_add_f32_e32 v105, v105, v64
	v_add_f32_e32 v145, v145, v65
	s_waitcnt lgkmcnt(5)
	v_mfma_f32_32x32x16_bf16 v[50:65], v[146:149], v[86:89], 0
	ds_read_b128 v[114:117], v183 offset:13376
	ds_read_b128 v[118:121], v183 offset:17984
	ds_read_b128 v[122:125], v183 offset:13408
	ds_read_b128 v[132:135], v183 offset:18016
	ds_read_b128 v[136:139], v183 offset:13440
	ds_read_b128 v[140:143], v183 offset:18048
	ds_read_b128 v[146:149], v183 offset:13472
	s_waitcnt lgkmcnt(11)
	v_mfma_f32_32x32x16_bf16 v[50:65], v[150:153], v[82:85], v[50:65]
	ds_read_b128 v[150:153], v183 offset:18080
	v_lshl_add_u64 v[112:113], v[112:113], 0, s[12:13]
	v_lshl_add_u64 v[110:111], v[110:111], 0, v[194:195]
	v_lshl_add_u64 v[108:109], v[108:109], 0, s[10:11]
	v_exp_f32_e32 v34, v34
	v_exp_f32_e32 v35, v35
	s_waitcnt lgkmcnt(11)
	v_mfma_f32_32x32x16_bf16 v[50:65], v[154:157], v[78:81], v[50:65]
	v_exp_f32_e32 v36, v36
	v_exp_f32_e32 v37, v37
	v_exp_f32_e32 v38, v38
	s_waitcnt lgkmcnt(10)
	v_mfma_f32_32x32x16_bf16 v[50:65], v[158:161], v[74:77], v[50:65]
	v_exp_f32_e32 v39, v39
	v_exp_f32_e32 v40, v40
	v_exp_f32_e32 v41, v41
	v_cvt_pk_bf16_f32 v154, v34, v35
	s_waitcnt lgkmcnt(9)
	v_mfma_f32_32x32x16_bf16 v[50:65], v[162:165], v[70:73], v[50:65]
	v_cvt_pk_bf16_f32 v155, v36, v37
	v_cvt_pk_bf16_f32 v156, v38, v39
	v_exp_f32_e32 v42, v42
	v_exp_f32_e32 v43, v43
	s_waitcnt lgkmcnt(8)
	v_mfma_f32_32x32x16_bf16 v[50:65], v[166:169], v[66:69], v[50:65]
	v_cvt_pk_bf16_f32 v157, v40, v41
	v_exp_f32_e32 v44, v44
	v_exp_f32_e32 v45, v45
	v_exp_f32_e32 v46, v46
	s_waitcnt lgkmcnt(7)
	v_mfma_f32_32x32x16_bf16 v[18:33], v[114:117], v[154:157], v[18:33]
	v_exp_f32_e32 v47, v47
	v_exp_f32_e32 v48, v48
	v_exp_f32_e32 v49, v49
	v_cvt_pk_bf16_f32 v158, v42, v43
	s_waitcnt lgkmcnt(6)
	v_mfma_f32_32x32x16_bf16 v[2:17], v[118:121], v[154:157], v[2:17]
	v_cvt_pk_bf16_f32 v159, v44, v45
	v_cvt_pk_bf16_f32 v160, v46, v47
	v_cvt_pk_bf16_f32 v161, v48, v49
	v_add_f32_e32 v105, v105, v34
	v_add_f32_e32 v145, v145, v35
	v_add_f32_e32 v105, v105, v36
	v_exp_f32_e32 v50, v50
	s_waitcnt lgkmcnt(5)
	v_mfma_f32_32x32x16_bf16 v[18:33], v[122:125], v[158:161], v[18:33]
	v_exp_f32_e32 v51, v51
	v_exp_f32_e32 v52, v52
	v_exp_f32_e32 v53, v53
	s_waitcnt lgkmcnt(4)
	v_mfma_f32_32x32x16_bf16 v[2:17], v[132:135], v[158:161], v[2:17]
	v_exp_f32_e32 v54, v54
	v_exp_f32_e32 v55, v55
	v_exp_f32_e32 v56, v56
	v_exp_f32_e32 v57, v57
	v_cvt_pk_bf16_f32 v162, v50, v51
	v_cvt_pk_bf16_f32 v163, v52, v53
	v_cvt_pk_bf16_f32 v164, v54, v55
	v_cvt_pk_bf16_f32 v165, v56, v57
	v_add_f32_e32 v145, v145, v37
	v_add_f32_e32 v105, v105, v38
	s_waitcnt lgkmcnt(3)
	v_mfma_f32_32x32x16_bf16 v[18:33], v[136:139], v[162:165], v[18:33]
	v_exp_f32_e32 v58, v58
	v_exp_f32_e32 v59, v59
	v_exp_f32_e32 v60, v60
	s_waitcnt lgkmcnt(2)
	v_mfma_f32_32x32x16_bf16 v[2:17], v[140:143], v[162:165], v[2:17]
	ds_read_b128 v[114:117], v182 offset:22592
	ds_read_b128 v[118:121], v182 offset:22624
	ds_read_b128 v[122:125], v182 offset:22656
	ds_read_b128 v[132:135], v182 offset:22688
	v_exp_f32_e32 v61, v61
	v_exp_f32_e32 v62, v62
	v_exp_f32_e32 v63, v63
	v_exp_f32_e32 v64, v64
	v_exp_f32_e32 v65, v65
	v_cvt_pk_bf16_f32 v166, v58, v59
	v_cvt_pk_bf16_f32 v167, v60, v61
	v_cvt_pk_bf16_f32 v168, v62, v63
	v_cvt_pk_bf16_f32 v169, v64, v65
	v_add_f32_e32 v145, v145, v39
	v_add_f32_e32 v105, v105, v40
	s_waitcnt lgkmcnt(5)
	v_mfma_f32_32x32x16_bf16 v[18:33], v[146:149], v[166:169], v[18:33]
	v_add_f32_e32 v145, v145, v41
	v_add_f32_e32 v105, v105, v42
	v_add_f32_e32 v145, v145, v43
	v_add_f32_e32 v105, v105, v44
	v_add_f32_e32 v145, v145, v45
	s_waitcnt lgkmcnt(4)
	v_mfma_f32_32x32x16_bf16 v[2:17], v[150:153], v[166:169], v[2:17]
	v_add_f32_e32 v105, v105, v46
	v_add_f32_e32 v145, v145, v47
	v_add_f32_e32 v105, v105, v48
	v_add_f32_e32 v145, v145, v49
	s_cmp_lt_u32 s31, s65
	s_cbranch_scc0 .Lfa_noload_11
	global_load_dwordx4 v[170:173], v[112:113], off
	global_load_dwordx4 v[174:177], v[110:111], off
	s_cmp_lg_u32 s43, 0
	s_cbranch_scc0 .Lfa_noload_11
	global_load_dwordx4 v[178:181], v[108:109], off
.Lfa_noload_11:
	ds_read_b128 v[136:139], v182 offset:22720
	ds_read_b128 v[140:143], v182 offset:22752
	ds_read_b128 v[146:149], v182 offset:29248
	ds_read_b128 v[150:153], v182 offset:29280
	s_waitcnt lgkmcnt(7)
	v_mfma_f32_32x32x16_bf16 v[34:49], v[114:117], v[86:89], 0
	v_add_f32_e32 v105, v105, v50
	v_add_f32_e32 v145, v145, v51
	v_add_f32_e32 v105, v105, v52
	ds_read_b128 v[154:157], v182 offset:29312
	s_waitcnt lgkmcnt(7)
	v_mfma_f32_32x32x16_bf16 v[34:49], v[118:121], v[82:85], v[34:49]
	v_add_f32_e32 v145, v145, v53
	v_add_f32_e32 v105, v105, v54
	v_add_f32_e32 v145, v145, v55
	ds_read_b128 v[158:161], v182 offset:29344
	s_waitcnt lgkmcnt(7)
	v_mfma_f32_32x32x16_bf16 v[34:49], v[122:125], v[78:81], v[34:49]
	v_add_f32_e32 v105, v105, v56
	v_add_f32_e32 v145, v145, v57
	v_add_f32_e32 v105, v105, v58
	ds_read_b128 v[162:165], v182 offset:29376
	s_waitcnt lgkmcnt(7)
	v_mfma_f32_32x32x16_bf16 v[34:49], v[132:135], v[74:77], v[34:49]
	v_add_f32_e32 v145, v145, v59
	v_add_f32_e32 v105, v105, v60
	v_add_f32_e32 v145, v145, v61
	ds_read_b128 v[166:169], v182 offset:29408
	s_waitcnt lgkmcnt(7)
	v_mfma_f32_32x32x16_bf16 v[34:49], v[136:139], v[70:73], v[34:49]
	v_add_f32_e32 v105, v105, v62
	v_add_f32_e32 v145, v145, v63
	s_waitcnt lgkmcnt(6)
	v_mfma_f32_32x32x16_bf16 v[34:49], v[140:143], v[66:69], v[34:49]
	v_add_f32_e32 v105, v105, v64
	v_add_f32_e32 v145, v145, v65
	s_waitcnt lgkmcnt(5)
	v_mfma_f32_32x32x16_bf16 v[50:65], v[146:149], v[86:89], 0
	ds_read_b128 v[114:117], v183 offset:35904
	ds_read_b128 v[118:121], v183 offset:40512
	ds_read_b128 v[122:125], v183 offset:35936
	ds_read_b128 v[132:135], v183 offset:40544
	ds_read_b128 v[136:139], v183 offset:35968
	ds_read_b128 v[140:143], v183 offset:40576
	ds_read_b128 v[146:149], v183 offset:36000
	s_waitcnt lgkmcnt(11)
	v_mfma_f32_32x32x16_bf16 v[50:65], v[150:153], v[82:85], v[50:65]
	ds_read_b128 v[150:153], v183 offset:40608
	v_lshl_add_u64 v[112:113], v[112:113], 0, s[12:13]
	v_lshl_add_u64 v[110:111], v[110:111], 0, v[194:195]
	v_lshl_add_u64 v[108:109], v[108:109], 0, s[10:11]
	v_exp_f32_e32 v34, v34
	v_exp_f32_e32 v35, v35
	s_waitcnt lgkmcnt(11)
	v_mfma_f32_32x32x16_bf16 v[50:65], v[154:157], v[78:81], v[50:65]
	v_exp_f32_e32 v36, v36
	v_exp_f32_e32 v37, v37
	v_exp_f32_e32 v38, v38
	s_waitcnt lgkmcnt(10)
	v_mfma_f32_32x32x16_bf16 v[50:65], v[158:161], v[74:77], v[50:65]
	v_exp_f32_e32 v39, v39
	v_exp_f32_e32 v40, v40
	v_exp_f32_e32 v41, v41
	v_cvt_pk_bf16_f32 v154, v34, v35
	s_waitcnt lgkmcnt(9)
	v_mfma_f32_32x32x16_bf16 v[50:65], v[162:165], v[70:73], v[50:65]
	v_cvt_pk_bf16_f32 v155, v36, v37
	v_cvt_pk_bf16_f32 v156, v38, v39
	v_exp_f32_e32 v42, v42
	v_exp_f32_e32 v43, v43
	s_waitcnt lgkmcnt(8)
	v_mfma_f32_32x32x16_bf16 v[50:65], v[166:169], v[66:69], v[50:65]
	v_cvt_pk_bf16_f32 v157, v40, v41
	v_exp_f32_e32 v44, v44
	v_exp_f32_e32 v45, v45
	v_exp_f32_e32 v46, v46
	s_waitcnt lgkmcnt(7)
	v_mfma_f32_32x32x16_bf16 v[18:33], v[114:117], v[154:157], v[18:33]
	v_exp_f32_e32 v47, v47
	v_exp_f32_e32 v48, v48
	v_exp_f32_e32 v49, v49
	v_cvt_pk_bf16_f32 v158, v42, v43
	s_waitcnt lgkmcnt(6)
	v_mfma_f32_32x32x16_bf16 v[2:17], v[118:121], v[154:157], v[2:17]
	v_cvt_pk_bf16_f32 v159, v44, v45
	v_cvt_pk_bf16_f32 v160, v46, v47
	v_cvt_pk_bf16_f32 v161, v48, v49
	v_add_f32_e32 v105, v105, v34
	v_add_f32_e32 v145, v145, v35
	v_add_f32_e32 v105, v105, v36
	v_exp_f32_e32 v50, v50
	s_waitcnt lgkmcnt(5)
	v_mfma_f32_32x32x16_bf16 v[18:33], v[122:125], v[158:161], v[18:33]
	v_exp_f32_e32 v51, v51
	v_exp_f32_e32 v52, v52
	v_exp_f32_e32 v53, v53
	s_waitcnt lgkmcnt(4)
	v_mfma_f32_32x32x16_bf16 v[2:17], v[132:135], v[158:161], v[2:17]
	v_exp_f32_e32 v54, v54
	v_exp_f32_e32 v55, v55
	v_exp_f32_e32 v56, v56
	v_exp_f32_e32 v57, v57
	v_cvt_pk_bf16_f32 v162, v50, v51
	v_cvt_pk_bf16_f32 v163, v52, v53
	v_cvt_pk_bf16_f32 v164, v54, v55
	v_cvt_pk_bf16_f32 v165, v56, v57
	v_add_f32_e32 v145, v145, v37
	v_add_f32_e32 v105, v105, v38
	s_waitcnt lgkmcnt(3)
	v_mfma_f32_32x32x16_bf16 v[18:33], v[136:139], v[162:165], v[18:33]
	v_exp_f32_e32 v58, v58
	v_exp_f32_e32 v59, v59
	v_exp_f32_e32 v60, v60
	s_waitcnt lgkmcnt(2)
	v_mfma_f32_32x32x16_bf16 v[2:17], v[140:143], v[162:165], v[2:17]
	v_exp_f32_e32 v61, v61
	v_exp_f32_e32 v62, v62
	v_exp_f32_e32 v63, v63
	v_exp_f32_e32 v64, v64
	v_exp_f32_e32 v65, v65
	v_cvt_pk_bf16_f32 v166, v58, v59
	v_cvt_pk_bf16_f32 v167, v60, v61
	v_cvt_pk_bf16_f32 v168, v62, v63
	v_cvt_pk_bf16_f32 v169, v64, v65
	v_add_f32_e32 v145, v145, v39
	v_add_f32_e32 v105, v105, v40
	s_waitcnt lgkmcnt(1)
	v_mfma_f32_32x32x16_bf16 v[18:33], v[146:149], v[166:169], v[18:33]
	v_add_f32_e32 v145, v145, v41
	v_add_f32_e32 v105, v105, v42
	v_add_f32_e32 v145, v145, v43
	v_add_f32_e32 v105, v105, v44
	v_add_f32_e32 v145, v145, v45
	s_waitcnt lgkmcnt(0)
	v_mfma_f32_32x32x16_bf16 v[2:17], v[150:153], v[166:169], v[2:17]
	v_add_f32_e32 v105, v105, v46
	v_add_f32_e32 v145, v145, v47
	v_add_f32_e32 v105, v105, v48
	v_add_f32_e32 v145, v145, v49
	s_cmp_lt_u32 s31, s65
	s_cbranch_scc0 .Lfa_nowrite_1
	s_waitcnt vmcnt(0)
	ds_write_b128 v106, v[98:101] offset:64
	ds_write_b128 v128, v[94:97] offset:64
	ds_write_b128 v106, v[170:173] offset:22592
	ds_write_b128 v128, v[174:177] offset:22592
	s_cmp_lg_u32 s43, 0
	s_cbranch_scc0 .Lfa_nowrite_1
	ds_write_b128 v129, v[90:93] offset:13376
	ds_write_b128 v129, v[178:181] offset:35904
